# up-GEMM epilogue: fp8 pairs converted straight into the store's register pair (16 moves and 3 pads fewer per unit)
# speedup vs baseline: 1.0070x; 1.0028x over previous
.LBB0_1916:
	s_mov_b32 s29, 0
	v_mov_b32_e32 v4, v166
	v_mov_b32_e32 v2, v167
	v_mov_b32_e32 v3, s24
	s_add_u32 s40, s2, 0xffffff00
	ds_read_b32 v3, v3 offset:288
	s_addc_u32 s41, s23, -1
	s_lshl_b32 s2, s31, 11
	s_add_i32 s2, s2, 0
	v_lshl_add_u32 v18, v2, 3, s83
	s_add_i32 s2, s2, 0x21000
	v_lshl_add_u32 v5, v18, 3, s2
	ds_read_b128 v[14:17], v5
	s_waitcnt lgkmcnt(1)
	v_readfirstlane_b32 s8, v3
	s_lshl_b32 s8, s8, 2
	s_add_i32 s8, s8, 0
	s_add_i32 s8, s8, 0x201c0
	v_mov_b32_e32 v2, s8
	ds_read2_b32 v[2:3], v2 offset1:32
	v_add_u32_e32 v19, s82, v4
	ds_read_b128 v[10:13], v5 offset:16
	ds_read_b128 v[6:9], v5 offset:32
	v_add_u32_e32 v22, 16, v19
	v_add_u32_e32 v24, 32, v19
	s_waitcnt lgkmcnt(2)
	v_readfirstlane_b32 s9, v2
	v_lshl_add_u32 v2, v19, 2, s2
	ds_read_b32 v20, v2 offset:1024
	v_readfirstlane_b32 s8, v3
	s_sub_i32 s8, s36, s8
	v_lshl_add_u32 v23, v22, 2, s2
	v_lshl_add_u32 v25, v24, 2, s2
	s_lshl_b32 s8, s8, 8
	ds_read_b128 v[2:5], v5 offset:48
	ds_read_b32 v23, v23 offset:1024
	ds_read_b32 v25, v25 offset:1024
	v_add_u32_e32 v21, s8, v19
	s_waitcnt lgkmcnt(3)
	v_mul_f32_e32 v20, 0x3b800000, v20
	v_cmp_gt_i32_e32 vcc, s9, v21
	s_waitcnt lgkmcnt(1)
	v_mul_f32_e32 v21, 0x3b800000, v23
	v_add_u32_e32 v26, 0xa0, v19
	v_cndmask_b32_e32 v180, 0, v20, vcc
	v_add_u32_e32 v20, s8, v22
	v_cmp_gt_i32_e32 vcc, s9, v20
	v_add_u32_e32 v20, s8, v24
	v_add_u32_e32 v22, 0x80, v19
	v_cndmask_b32_e32 v164, 0, v21, vcc
	s_waitcnt lgkmcnt(0)
	v_mul_f32_e32 v21, 0x3b800000, v25
	v_cmp_gt_i32_e32 vcc, s9, v20
	v_add_u32_e32 v20, 48, v19
	v_add_u32_e32 v24, 0x90, v19
	v_cndmask_b32_e32 v162, 0, v21, vcc
	v_lshl_add_u32 v21, v20, 2, s2
	v_lshl_add_u32 v23, v22, 2, s2
	v_lshl_add_u32 v25, v24, 2, s2
	v_lshl_add_u32 v27, v26, 2, s2
	v_add_u32_e32 v29, 0xb0, v19
	v_add_u32_e32 v20, s8, v20
	v_lshl_add_u32 v28, v29, 2, s2
	ds_read_b32 v21, v21 offset:1024
	ds_read_b32 v23, v23 offset:1024
	ds_read_b32 v25, v25 offset:1024
	ds_read_b32 v27, v27 offset:1024
	ds_read_b32 v31, v28 offset:1024
	s_waitcnt lgkmcnt(4)
	v_mul_f32_e32 v21, 0x3b800000, v21
	v_cmp_gt_i32_e32 vcc, s9, v20
	v_add_u32_e32 v20, s8, v22
	s_lshl_b32 s42, s14, 7
	v_cndmask_b32_e32 v32, 0, v21, vcc
	s_waitcnt lgkmcnt(3)
	v_mul_f32_e32 v21, 0x3b800000, v23
	v_cmp_gt_i32_e32 vcc, s9, v20
	v_add_u32_e32 v20, s8, v24
	v_mov_b32_e32 v24, v14
	v_cndmask_b32_e32 v30, 0, v21, vcc
	s_waitcnt lgkmcnt(2)
	v_mul_f32_e32 v21, 0x3b800000, v25
	v_mov_b32_e32 v25, v16
	v_pk_fma_f32 v[182:183], v[158:159], v[180:181], v[24:25] op_sel_hi:[1,0,1]
	v_mov_b32_e32 v16, v15
	v_min_f32_e32 v182, 0x40e00000, v182
	v_min_f32_e32 v183, 0x40e00000, v183
	v_pk_mul_f32 v[184:185], v[182:183], s[20:21] op_sel_hi:[1,0]
	v_cmp_gt_i32_e32 vcc, s9, v20
	v_exp_f32_e32 v184, v184
	v_exp_f32_e32 v185, v185
	v_add_u32_e32 v20, s8, v26
	v_cndmask_b32_e32 v28, 0, v21, vcc
	s_waitcnt lgkmcnt(1)
	v_mul_f32_e32 v21, 0x3b800000, v27
	v_pk_add_f32 v[14:15], v[184:185], 1.0 op_sel_hi:[1,0]
	v_pk_fma_f32 v[184:185], v[126:127], v[180:181], v[16:17] op_sel_hi:[1,0,1]
	v_rcp_f32_e32 v14, v14
	v_rcp_f32_e32 v15, v15
	v_med3_f32 v184, v184, s37, v176
	v_med3_f32 v185, v185, s37, v176
	v_cmp_gt_i32_e32 vcc, s9, v20
	v_pk_mul_f32 v[14:15], v[182:183], v[14:15]
	v_add_u32_e32 v20, s8, v29
	v_pk_fma_f32 v[182:183], v[184:185], v[14:15], v[14:15]
	v_mov_b32_e32 v14, v10
	v_mov_b32_e32 v15, v12
	v_pk_fma_f32 v[184:185], v[160:161], v[180:181], v[14:15] op_sel_hi:[1,0,1]
	v_mov_b32_e32 v12, v11
	v_min_f32_e32 v184, 0x40e00000, v184
	v_min_f32_e32 v185, 0x40e00000, v185
	v_pk_mul_f32 v[186:187], v[184:185], s[20:21] op_sel_hi:[1,0]
	v_cndmask_b32_e32 v26, 0, v21, vcc
	v_exp_f32_e32 v186, v186
	v_exp_f32_e32 v187, v187
	s_waitcnt lgkmcnt(0)
	v_mul_f32_e32 v21, 0x3b800000, v31
	v_cmp_gt_i32_e32 vcc, s9, v20
	v_pk_add_f32 v[10:11], v[186:187], 1.0 op_sel_hi:[1,0]
	v_cndmask_b32_e32 v22, 0, v21, vcc
	v_rcp_f32_e32 v10, v10
	v_rcp_f32_e32 v11, v11
	v_cvt_pk_fp8_f32 v192, v182, v183
	v_pk_fma_f32 v[182:183], v[128:129], v[180:181], v[12:13] op_sel_hi:[1,0,1]
	v_pk_mul_f32 v[10:11], v[184:185], v[10:11]
	v_med3_f32 v182, v182, s37, v176
	v_med3_f32 v183, v183, s37, v176
	v_pk_fma_f32 v[182:183], v[182:183], v[10:11], v[10:11]
	v_mov_b32_e32 v10, v6
	v_mov_b32_e32 v11, v8
	v_pk_fma_f32 v[184:185], v[154:155], v[180:181], v[10:11] op_sel_hi:[1,0,1]
	v_mov_b32_e32 v8, v7
	v_min_f32_e32 v184, 0x40e00000, v184
	v_min_f32_e32 v185, 0x40e00000, v185
	v_pk_mul_f32 v[186:187], v[184:185], s[20:21] op_sel_hi:[1,0]
	v_cvt_pk_fp8_f32 v192, v182, v183 op_sel:[0,0,1]
	v_exp_f32_e32 v186, v186
	v_exp_f32_e32 v187, v187
	v_pk_fma_f32 v[182:183], v[122:123], v[180:181], v[8:9] op_sel_hi:[1,0,1]
	v_med3_f32 v182, v182, s37, v176
	v_pk_add_f32 v[6:7], v[186:187], 1.0 op_sel_hi:[1,0]
	v_med3_f32 v183, v183, s37, v176
	v_rcp_f32_e32 v6, v6
	v_rcp_f32_e32 v7, v7
	v_lshl_add_u32 v20, s36, 8, v19
	s_ashr_i32 s43, s42, 31
	v_pk_mul_f32 v[6:7], v[184:185], v[6:7]
	v_ashrrev_i32_e32 v19, 31, v18
	v_pk_fma_f32 v[182:183], v[182:183], v[6:7], v[6:7]
	v_mov_b32_e32 v6, v2
	v_mov_b32_e32 v7, v4
	v_pk_fma_f32 v[184:185], v[156:157], v[180:181], v[6:7] op_sel_hi:[1,0,1]
	v_mov_b32_e32 v4, v3
	v_min_f32_e32 v184, 0x40e00000, v184
	v_min_f32_e32 v185, 0x40e00000, v185
	v_pk_mul_f32 v[186:187], v[184:185], s[20:21] op_sel_hi:[1,0]
	v_pk_fma_f32 v[180:181], v[124:125], v[180:181], v[4:5] op_sel_hi:[1,0,1]
	v_exp_f32_e32 v186, v186
	v_exp_f32_e32 v187, v187
	v_cvt_pk_fp8_f32 v193, v182, v183
	v_med3_f32 v180, v180, s37, v176
	v_med3_f32 v181, v181, s37, v176
	v_pk_add_f32 v[2:3], v[186:187], 1.0 op_sel_hi:[1,0]
	v_pk_fma_f32 v[182:183], v[150:151], v[164:165], v[24:25] op_sel_hi:[1,0,1]
	v_rcp_f32_e32 v2, v2
	v_rcp_f32_e32 v3, v3
	v_min_f32_e32 v182, 0x40e00000, v182
	v_min_f32_e32 v183, 0x40e00000, v183
	s_and_b64 vcc, exec, s[6:7]
	v_pk_mul_f32 v[2:3], v[184:185], v[2:3]
	v_pk_mul_f32 v[184:185], v[182:183], s[20:21] op_sel_hi:[1,0]
	v_pk_fma_f32 v[2:3], v[180:181], v[2:3], v[2:3]
	v_exp_f32_e32 v184, v184
	v_cvt_pk_fp8_f32 v193, v2, v3 op_sel:[0,0,1]
	v_ashrrev_i32_e32 v21, 31, v20
	v_lshlrev_b64 v[180:181], 10, v[20:21]
	v_exp_f32_e32 v185, v185
	v_lshl_add_u64 v[180:181], s[12:13], 0, v[180:181]
	v_lshl_add_u64 v[180:181], v[180:181], 0, s[42:43]
	v_lshl_add_u64 v[188:189], v[180:181], 0, v[18:19]
	global_store_dwordx2 v[188:189], v[192:193], off
	v_pk_add_f32 v[2:3], v[184:185], 1.0 op_sel_hi:[1,0]
	v_pk_fma_f32 v[180:181], v[118:119], v[164:165], v[16:17] op_sel_hi:[1,0,1]
	v_rcp_f32_e32 v2, v2
	v_rcp_f32_e32 v3, v3
	v_med3_f32 v180, v180, s37, v176
	v_med3_f32 v181, v181, s37, v176
	v_pk_mul_f32 v[2:3], v[182:183], v[2:3]
	v_pk_fma_f32 v[182:183], v[152:153], v[164:165], v[14:15] op_sel_hi:[1,0,1]
	v_pk_fma_f32 v[2:3], v[180:181], v[2:3], v[2:3]
	v_min_f32_e32 v182, 0x40e00000, v182
	v_min_f32_e32 v183, 0x40e00000, v183
	v_pk_mul_f32 v[184:185], v[182:183], s[20:21] op_sel_hi:[1,0]
	v_cvt_pk_fp8_f32 v194, v2, v3
	v_exp_f32_e32 v184, v184
	v_exp_f32_e32 v185, v185
	v_pk_fma_f32 v[180:181], v[120:121], v[164:165], v[12:13] op_sel_hi:[1,0,1]
	v_med3_f32 v180, v180, s37, v176
	v_pk_add_f32 v[2:3], v[184:185], 1.0 op_sel_hi:[1,0]
	v_med3_f32 v181, v181, s37, v176
	v_rcp_f32_e32 v2, v2
	v_rcp_f32_e32 v3, v3
	s_nop 0
	v_pk_mul_f32 v[2:3], v[182:183], v[2:3]
	v_pk_fma_f32 v[182:183], v[146:147], v[164:165], v[10:11] op_sel_hi:[1,0,1]
	v_pk_fma_f32 v[2:3], v[180:181], v[2:3], v[2:3]
	v_min_f32_e32 v182, 0x40e00000, v182
	v_min_f32_e32 v183, 0x40e00000, v183
	v_pk_mul_f32 v[184:185], v[182:183], s[20:21] op_sel_hi:[1,0]
	v_cvt_pk_fp8_f32 v194, v2, v3 op_sel:[0,0,1]
	v_exp_f32_e32 v184, v184
	v_exp_f32_e32 v185, v185
	v_pk_fma_f32 v[180:181], v[114:115], v[164:165], v[8:9] op_sel_hi:[1,0,1]
	v_pk_add_f32 v[2:3], v[184:185], 1.0 op_sel_hi:[1,0]
	s_nop 0
	v_rcp_f32_e32 v2, v2
	v_rcp_f32_e32 v3, v3
	v_med3_f32 v180, v180, s37, v176
	v_med3_f32 v181, v181, s37, v176
	v_pk_mul_f32 v[2:3], v[182:183], v[2:3]
	v_pk_fma_f32 v[182:183], v[148:149], v[164:165], v[6:7] op_sel_hi:[1,0,1]
	v_pk_fma_f32 v[2:3], v[180:181], v[2:3], v[2:3]
	v_min_f32_e32 v182, 0x40e00000, v182
	v_min_f32_e32 v183, 0x40e00000, v183
	v_pk_mul_f32 v[184:185], v[182:183], s[20:21] op_sel_hi:[1,0]
	v_cvt_pk_fp8_f32 v195, v2, v3
	v_exp_f32_e32 v184, v184
	v_exp_f32_e32 v185, v185
	v_pk_fma_f32 v[180:181], v[116:117], v[164:165], v[4:5] op_sel_hi:[1,0,1]
	v_pk_add_f32 v[2:3], v[184:185], 1.0 op_sel_hi:[1,0]
	s_nop 0
	v_rcp_f32_e32 v2, v2
	v_rcp_f32_e32 v3, v3
	v_med3_f32 v180, v180, s37, v176
	v_med3_f32 v181, v181, s37, v176
	v_pk_mul_f32 v[2:3], v[182:183], v[2:3]
	v_pk_fma_f32 v[182:183], v[142:143], v[162:163], v[24:25] op_sel_hi:[1,0,1]
	v_pk_fma_f32 v[2:3], v[180:181], v[2:3], v[2:3]
	v_min_f32_e32 v182, 0x40e00000, v182
	v_min_f32_e32 v183, 0x40e00000, v183
	v_cvt_pk_fp8_f32 v195, v2, v3 op_sel:[0,0,1]
	v_pk_mul_f32 v[184:185], v[182:183], s[20:21] op_sel_hi:[1,0]
	v_exp_f32_e32 v184, v184
	v_exp_f32_e32 v185, v185
	s_mov_b32 s28, 0x4000
	v_lshl_add_u64 v[180:181], v[188:189], 0, s[28:29]
	global_store_dwordx2 v[180:181], v[194:195], off
	v_pk_add_f32 v[2:3], v[184:185], 1.0 op_sel_hi:[1,0]
	v_pk_fma_f32 v[180:181], v[110:111], v[162:163], v[16:17] op_sel_hi:[1,0,1]
	v_rcp_f32_e32 v2, v2
	v_rcp_f32_e32 v3, v3
	v_med3_f32 v180, v180, s37, v176
	v_med3_f32 v181, v181, s37, v176
	v_pk_mul_f32 v[2:3], v[182:183], v[2:3]
	v_pk_fma_f32 v[182:183], v[144:145], v[162:163], v[14:15] op_sel_hi:[1,0,1]
	v_pk_fma_f32 v[2:3], v[180:181], v[2:3], v[2:3]
	v_min_f32_e32 v182, 0x40e00000, v182
	v_min_f32_e32 v183, 0x40e00000, v183
	v_pk_mul_f32 v[184:185], v[182:183], s[20:21] op_sel_hi:[1,0]
	v_cvt_pk_fp8_f32 v196, v2, v3
	v_exp_f32_e32 v184, v184
	v_exp_f32_e32 v185, v185
	v_pk_fma_f32 v[180:181], v[112:113], v[162:163], v[12:13] op_sel_hi:[1,0,1]
	v_med3_f32 v180, v180, s37, v176
	v_pk_add_f32 v[2:3], v[184:185], 1.0 op_sel_hi:[1,0]
	v_med3_f32 v181, v181, s37, v176
	v_rcp_f32_e32 v2, v2
	v_rcp_f32_e32 v3, v3
	s_nop 0
	v_pk_mul_f32 v[2:3], v[182:183], v[2:3]
	v_pk_fma_f32 v[182:183], v[138:139], v[162:163], v[10:11] op_sel_hi:[1,0,1]
	v_pk_fma_f32 v[2:3], v[180:181], v[2:3], v[2:3]
	v_min_f32_e32 v182, 0x40e00000, v182
	v_min_f32_e32 v183, 0x40e00000, v183
	v_pk_mul_f32 v[184:185], v[182:183], s[20:21] op_sel_hi:[1,0]
	v_cvt_pk_fp8_f32 v196, v2, v3 op_sel:[0,0,1]
	v_exp_f32_e32 v184, v184
	v_exp_f32_e32 v185, v185
	v_pk_fma_f32 v[180:181], v[106:107], v[162:163], v[8:9] op_sel_hi:[1,0,1]
	v_pk_add_f32 v[2:3], v[184:185], 1.0 op_sel_hi:[1,0]
	s_nop 0
	v_rcp_f32_e32 v2, v2
	v_rcp_f32_e32 v3, v3
	v_med3_f32 v180, v180, s37, v176
	v_med3_f32 v181, v181, s37, v176
	v_pk_mul_f32 v[2:3], v[182:183], v[2:3]
	v_pk_fma_f32 v[182:183], v[140:141], v[162:163], v[6:7] op_sel_hi:[1,0,1]
	v_pk_fma_f32 v[2:3], v[180:181], v[2:3], v[2:3]
	v_min_f32_e32 v182, 0x40e00000, v182
	v_min_f32_e32 v183, 0x40e00000, v183
	v_pk_mul_f32 v[184:185], v[182:183], s[20:21] op_sel_hi:[1,0]
	v_cvt_pk_fp8_f32 v197, v2, v3
	v_exp_f32_e32 v184, v184
	v_exp_f32_e32 v185, v185
	v_pk_fma_f32 v[180:181], v[108:109], v[162:163], v[4:5] op_sel_hi:[1,0,1]
	v_pk_add_f32 v[2:3], v[184:185], 1.0 op_sel_hi:[1,0]
	s_nop 0
	v_rcp_f32_e32 v2, v2
	v_rcp_f32_e32 v3, v3
	v_med3_f32 v180, v180, s37, v176
	v_med3_f32 v181, v181, s37, v176
	v_pk_mul_f32 v[2:3], v[182:183], v[2:3]
	v_pk_fma_f32 v[182:183], v[134:135], v[32:33], v[24:25] op_sel_hi:[1,0,1]
	v_pk_fma_f32 v[2:3], v[180:181], v[2:3], v[2:3]
	v_min_f32_e32 v182, 0x40e00000, v182
	v_min_f32_e32 v183, 0x40e00000, v183
	v_cvt_pk_fp8_f32 v197, v2, v3 op_sel:[0,0,1]
	v_pk_mul_f32 v[184:185], v[182:183], s[20:21] op_sel_hi:[1,0]
	v_exp_f32_e32 v184, v184
	v_exp_f32_e32 v185, v185
	s_mov_b32 s28, 0x8000
	v_lshl_add_u64 v[180:181], v[188:189], 0, s[28:29]
	global_store_dwordx2 v[180:181], v[196:197], off
	v_pk_add_f32 v[2:3], v[184:185], 1.0 op_sel_hi:[1,0]
	v_pk_fma_f32 v[180:181], v[102:103], v[32:33], v[16:17] op_sel_hi:[1,0,1]
	v_rcp_f32_e32 v2, v2
	v_rcp_f32_e32 v3, v3
	v_med3_f32 v180, v180, s37, v176
	v_med3_f32 v181, v181, s37, v176
	v_pk_mul_f32 v[2:3], v[182:183], v[2:3]
	v_pk_fma_f32 v[182:183], v[136:137], v[32:33], v[14:15] op_sel_hi:[1,0,1]
	v_pk_fma_f32 v[2:3], v[180:181], v[2:3], v[2:3]
	v_min_f32_e32 v182, 0x40e00000, v182
	v_min_f32_e32 v183, 0x40e00000, v183
	v_pk_mul_f32 v[184:185], v[182:183], s[20:21] op_sel_hi:[1,0]
	v_cvt_pk_fp8_f32 v198, v2, v3
	v_exp_f32_e32 v184, v184
	v_exp_f32_e32 v185, v185
	v_pk_fma_f32 v[180:181], v[104:105], v[32:33], v[12:13] op_sel_hi:[1,0,1]
	v_med3_f32 v180, v180, s37, v176
	v_pk_add_f32 v[2:3], v[184:185], 1.0 op_sel_hi:[1,0]
	v_med3_f32 v181, v181, s37, v176
	v_rcp_f32_e32 v2, v2
	v_rcp_f32_e32 v3, v3
	s_nop 0
	v_pk_mul_f32 v[2:3], v[182:183], v[2:3]
	v_pk_fma_f32 v[182:183], v[130:131], v[32:33], v[10:11] op_sel_hi:[1,0,1]
	v_pk_fma_f32 v[2:3], v[180:181], v[2:3], v[2:3]
	v_min_f32_e32 v182, 0x40e00000, v182
	v_min_f32_e32 v183, 0x40e00000, v183
	v_pk_mul_f32 v[184:185], v[182:183], s[20:21] op_sel_hi:[1,0]
	v_cvt_pk_fp8_f32 v198, v2, v3 op_sel:[0,0,1]
	v_exp_f32_e32 v184, v184
	v_exp_f32_e32 v185, v185
	v_pk_fma_f32 v[180:181], v[98:99], v[32:33], v[8:9] op_sel_hi:[1,0,1]
	v_pk_add_f32 v[2:3], v[184:185], 1.0 op_sel_hi:[1,0]
	s_nop 0
	v_rcp_f32_e32 v2, v2
	v_rcp_f32_e32 v3, v3
	v_med3_f32 v180, v180, s37, v176
	v_med3_f32 v181, v181, s37, v176
	v_pk_mul_f32 v[2:3], v[182:183], v[2:3]
	v_pk_fma_f32 v[182:183], v[132:133], v[32:33], v[6:7] op_sel_hi:[1,0,1]
	v_pk_fma_f32 v[2:3], v[180:181], v[2:3], v[2:3]
	v_min_f32_e32 v182, 0x40e00000, v182
	v_min_f32_e32 v183, 0x40e00000, v183
	v_pk_mul_f32 v[184:185], v[182:183], s[20:21] op_sel_hi:[1,0]
	v_cvt_pk_fp8_f32 v199, v2, v3
	v_exp_f32_e32 v184, v184
	v_exp_f32_e32 v185, v185
	v_pk_fma_f32 v[32:33], v[100:101], v[32:33], v[4:5] op_sel_hi:[1,0,1]
	v_pk_fma_f32 v[180:181], v[94:95], v[30:31], v[24:25] op_sel_hi:[1,0,1]
	v_med3_f32 v32, v32, s37, v176
	v_pk_add_f32 v[2:3], v[184:185], 1.0 op_sel_hi:[1,0]
	v_med3_f32 v33, v33, s37, v176
	v_rcp_f32_e32 v2, v2
	v_rcp_f32_e32 v3, v3
	v_min_f32_e32 v180, 0x40e00000, v180
	v_min_f32_e32 v181, 0x40e00000, v181
	v_pk_mul_f32 v[2:3], v[182:183], v[2:3]
	s_nop 0
	v_pk_fma_f32 v[2:3], v[32:33], v[2:3], v[2:3]
	v_cvt_pk_fp8_f32 v199, v2, v3 op_sel:[0,0,1]
	v_pk_mul_f32 v[182:183], v[180:181], s[20:21] op_sel_hi:[1,0]
	v_exp_f32_e32 v182, v182
	v_exp_f32_e32 v183, v183
	s_mov_b32 s28, 0xc000
	v_lshl_add_u64 v[32:33], v[188:189], 0, s[28:29]
	global_store_dwordx2 v[32:33], v[198:199], off
	v_pk_add_f32 v[32:33], v[182:183], 1.0 op_sel_hi:[1,0]
	v_pk_fma_f32 v[182:183], v[62:63], v[30:31], v[16:17] op_sel_hi:[1,0,1]
	v_rcp_f32_e32 v32, v32
	v_rcp_f32_e32 v33, v33
	v_med3_f32 v182, v182, s37, v176
	v_med3_f32 v183, v183, s37, v176
	v_pk_mul_f32 v[32:33], v[180:181], v[32:33]
	v_pk_fma_f32 v[180:181], v[96:97], v[30:31], v[14:15] op_sel_hi:[1,0,1]
	v_pk_fma_f32 v[32:33], v[182:183], v[32:33], v[32:33]
	v_min_f32_e32 v180, 0x40e00000, v180
	v_min_f32_e32 v181, 0x40e00000, v181
	v_pk_mul_f32 v[184:185], v[180:181], s[20:21] op_sel_hi:[1,0]
	v_cvt_pk_fp8_f32 v200, v32, v33
	v_exp_f32_e32 v184, v184
	v_exp_f32_e32 v185, v185
	v_pk_fma_f32 v[182:183], v[64:65], v[30:31], v[12:13] op_sel_hi:[1,0,1]
	v_med3_f32 v182, v182, s37, v176
	v_pk_add_f32 v[32:33], v[184:185], 1.0 op_sel_hi:[1,0]
	v_med3_f32 v183, v183, s37, v176
	v_rcp_f32_e32 v32, v32
	v_rcp_f32_e32 v33, v33
	s_nop 0
	v_pk_mul_f32 v[32:33], v[180:181], v[32:33]
	v_pk_fma_f32 v[180:181], v[90:91], v[30:31], v[10:11] op_sel_hi:[1,0,1]
	v_pk_fma_f32 v[32:33], v[182:183], v[32:33], v[32:33]
	v_min_f32_e32 v180, 0x40e00000, v180
	v_min_f32_e32 v181, 0x40e00000, v181
	v_pk_mul_f32 v[184:185], v[180:181], s[20:21] op_sel_hi:[1,0]
	v_cvt_pk_fp8_f32 v200, v32, v33 op_sel:[0,0,1]
	v_exp_f32_e32 v184, v184
	v_exp_f32_e32 v185, v185
	v_pk_fma_f32 v[182:183], v[58:59], v[30:31], v[8:9] op_sel_hi:[1,0,1]
	v_med3_f32 v182, v182, s37, v176
	v_pk_add_f32 v[32:33], v[184:185], 1.0 op_sel_hi:[1,0]
	v_med3_f32 v183, v183, s37, v176
	v_rcp_f32_e32 v32, v32
	v_rcp_f32_e32 v33, v33
	s_nop 0
	v_pk_mul_f32 v[32:33], v[180:181], v[32:33]
	v_pk_fma_f32 v[180:181], v[92:93], v[30:31], v[6:7] op_sel_hi:[1,0,1]
	v_pk_fma_f32 v[32:33], v[182:183], v[32:33], v[32:33]
	v_min_f32_e32 v180, 0x40e00000, v180
	v_min_f32_e32 v181, 0x40e00000, v181
	v_pk_mul_f32 v[184:185], v[180:181], s[20:21] op_sel_hi:[1,0]
	v_cvt_pk_fp8_f32 v201, v32, v33
	v_exp_f32_e32 v184, v184
	v_exp_f32_e32 v185, v185
	v_pk_fma_f32 v[30:31], v[60:61], v[30:31], v[4:5] op_sel_hi:[1,0,1]
	v_med3_f32 v30, v30, s37, v176
	v_pk_add_f32 v[32:33], v[184:185], 1.0 op_sel_hi:[1,0]
	v_med3_f32 v31, v31, s37, v176
	v_rcp_f32_e32 v32, v32
	v_rcp_f32_e32 v33, v33
	s_nop 0
	v_pk_mul_f32 v[32:33], v[180:181], v[32:33]
	s_nop 0
	v_pk_fma_f32 v[30:31], v[30:31], v[32:33], v[32:33]
	v_pk_fma_f32 v[32:33], v[86:87], v[28:29], v[24:25] op_sel_hi:[1,0,1]
	v_cvt_pk_fp8_f32 v201, v30, v31 op_sel:[0,0,1]
	v_min_f32_e32 v32, 0x40e00000, v32
	v_min_f32_e32 v33, 0x40e00000, v33
	v_pk_mul_f32 v[180:181], v[32:33], s[20:21] op_sel_hi:[1,0]
	v_exp_f32_e32 v180, v180
	v_exp_f32_e32 v181, v181
	s_mov_b32 s28, 0x20000
	v_lshl_add_u64 v[2:3], v[188:189], 0, s[28:29]
	global_store_dwordx2 v[2:3], v[200:201], off
	v_pk_add_f32 v[2:3], v[180:181], 1.0 op_sel_hi:[1,0]
	v_pk_fma_f32 v[30:31], v[54:55], v[28:29], v[16:17] op_sel_hi:[1,0,1]
	v_rcp_f32_e32 v2, v2
	v_rcp_f32_e32 v3, v3
	v_med3_f32 v30, v30, s37, v176
	v_med3_f32 v31, v31, s37, v176
	v_pk_mul_f32 v[2:3], v[32:33], v[2:3]
	v_pk_fma_f32 v[32:33], v[88:89], v[28:29], v[14:15] op_sel_hi:[1,0,1]
	v_pk_fma_f32 v[2:3], v[30:31], v[2:3], v[2:3]
	v_min_f32_e32 v32, 0x40e00000, v32
	v_min_f32_e32 v33, 0x40e00000, v33
	v_pk_mul_f32 v[180:181], v[32:33], s[20:21] op_sel_hi:[1,0]
	v_cvt_pk_fp8_f32 v202, v2, v3
	v_exp_f32_e32 v180, v180
	v_exp_f32_e32 v181, v181
	v_pk_fma_f32 v[30:31], v[56:57], v[28:29], v[12:13] op_sel_hi:[1,0,1]
	v_med3_f32 v30, v30, s37, v176
	v_pk_add_f32 v[2:3], v[180:181], 1.0 op_sel_hi:[1,0]
	v_med3_f32 v31, v31, s37, v176
	v_rcp_f32_e32 v2, v2
	v_rcp_f32_e32 v3, v3
	s_nop 0
	v_pk_mul_f32 v[2:3], v[32:33], v[2:3]
	v_pk_fma_f32 v[32:33], v[82:83], v[28:29], v[10:11] op_sel_hi:[1,0,1]
	v_pk_fma_f32 v[2:3], v[30:31], v[2:3], v[2:3]
	v_min_f32_e32 v32, 0x40e00000, v32
	v_min_f32_e32 v33, 0x40e00000, v33
	v_pk_mul_f32 v[180:181], v[32:33], s[20:21] op_sel_hi:[1,0]
	v_cvt_pk_fp8_f32 v202, v2, v3 op_sel:[0,0,1]
	v_exp_f32_e32 v180, v180
	v_exp_f32_e32 v181, v181
	v_pk_fma_f32 v[30:31], v[50:51], v[28:29], v[8:9] op_sel_hi:[1,0,1]
	v_pk_add_f32 v[2:3], v[180:181], 1.0 op_sel_hi:[1,0]
	s_nop 0
	v_rcp_f32_e32 v2, v2
	v_rcp_f32_e32 v3, v3
	v_med3_f32 v30, v30, s37, v176
	v_med3_f32 v31, v31, s37, v176
	v_pk_mul_f32 v[2:3], v[32:33], v[2:3]
	v_pk_fma_f32 v[32:33], v[84:85], v[28:29], v[6:7] op_sel_hi:[1,0,1]
	v_pk_fma_f32 v[2:3], v[30:31], v[2:3], v[2:3]
	v_min_f32_e32 v32, 0x40e00000, v32
	v_min_f32_e32 v33, 0x40e00000, v33
	v_pk_mul_f32 v[180:181], v[32:33], s[20:21] op_sel_hi:[1,0]
	v_cvt_pk_fp8_f32 v203, v2, v3
	v_exp_f32_e32 v180, v180
	v_exp_f32_e32 v181, v181
	v_pk_fma_f32 v[28:29], v[52:53], v[28:29], v[4:5] op_sel_hi:[1,0,1]
	v_pk_fma_f32 v[30:31], v[78:79], v[26:27], v[24:25] op_sel_hi:[1,0,1]
	v_med3_f32 v28, v28, s37, v176
	v_pk_add_f32 v[2:3], v[180:181], 1.0 op_sel_hi:[1,0]
	v_med3_f32 v29, v29, s37, v176
	v_rcp_f32_e32 v2, v2
	v_rcp_f32_e32 v3, v3
	v_min_f32_e32 v30, 0x40e00000, v30
	v_min_f32_e32 v31, 0x40e00000, v31
	v_pk_mul_f32 v[2:3], v[32:33], v[2:3]
	s_nop 0
	v_pk_fma_f32 v[2:3], v[28:29], v[2:3], v[2:3]
	v_cvt_pk_fp8_f32 v203, v2, v3 op_sel:[0,0,1]
	v_pk_mul_f32 v[32:33], v[30:31], s[20:21] op_sel_hi:[1,0]
	v_exp_f32_e32 v32, v32
	v_exp_f32_e32 v33, v33
	s_mov_b32 s28, 0x24000
	v_lshl_add_u64 v[28:29], v[188:189], 0, s[28:29]
	global_store_dwordx2 v[28:29], v[202:203], off
	v_pk_add_f32 v[2:3], v[32:33], 1.0 op_sel_hi:[1,0]
	v_pk_fma_f32 v[28:29], v[46:47], v[26:27], v[16:17] op_sel_hi:[1,0,1]
	v_rcp_f32_e32 v2, v2
	v_rcp_f32_e32 v3, v3
	v_med3_f32 v28, v28, s37, v176
	v_med3_f32 v29, v29, s37, v176
	v_pk_mul_f32 v[2:3], v[30:31], v[2:3]
	v_pk_fma_f32 v[30:31], v[80:81], v[26:27], v[14:15] op_sel_hi:[1,0,1]
	v_pk_fma_f32 v[2:3], v[28:29], v[2:3], v[2:3]
	v_min_f32_e32 v30, 0x40e00000, v30
	v_min_f32_e32 v31, 0x40e00000, v31
	v_pk_mul_f32 v[32:33], v[30:31], s[20:21] op_sel_hi:[1,0]
	v_cvt_pk_fp8_f32 v204, v2, v3
	v_exp_f32_e32 v32, v32
	v_exp_f32_e32 v33, v33
	v_pk_fma_f32 v[28:29], v[48:49], v[26:27], v[12:13] op_sel_hi:[1,0,1]
	v_med3_f32 v28, v28, s37, v176
	v_pk_add_f32 v[2:3], v[32:33], 1.0 op_sel_hi:[1,0]
	v_med3_f32 v29, v29, s37, v176
	v_rcp_f32_e32 v2, v2
	v_rcp_f32_e32 v3, v3
	s_nop 0
	v_pk_mul_f32 v[2:3], v[30:31], v[2:3]
	v_pk_fma_f32 v[30:31], v[74:75], v[26:27], v[10:11] op_sel_hi:[1,0,1]
	v_pk_fma_f32 v[2:3], v[28:29], v[2:3], v[2:3]
	v_min_f32_e32 v30, 0x40e00000, v30
	v_min_f32_e32 v31, 0x40e00000, v31
	v_pk_mul_f32 v[32:33], v[30:31], s[20:21] op_sel_hi:[1,0]
	v_cvt_pk_fp8_f32 v204, v2, v3 op_sel:[0,0,1]
	v_exp_f32_e32 v32, v32
	v_exp_f32_e32 v33, v33
	v_pk_fma_f32 v[28:29], v[42:43], v[26:27], v[8:9] op_sel_hi:[1,0,1]
	v_pk_fma_f32 v[24:25], v[70:71], v[22:23], v[24:25] op_sel_hi:[1,0,1]
	v_med3_f32 v28, v28, s37, v176
	v_pk_add_f32 v[2:3], v[32:33], 1.0 op_sel_hi:[1,0]
	v_med3_f32 v29, v29, s37, v176
	v_rcp_f32_e32 v2, v2
	v_rcp_f32_e32 v3, v3
	v_min_f32_e32 v24, 0x40e00000, v24
	v_min_f32_e32 v25, 0x40e00000, v25
	v_pk_fma_f32 v[14:15], v[72:73], v[22:23], v[14:15] op_sel_hi:[1,0,1]
	v_pk_mul_f32 v[2:3], v[30:31], v[2:3]
	v_pk_fma_f32 v[30:31], v[76:77], v[26:27], v[6:7] op_sel_hi:[1,0,1]
	v_pk_fma_f32 v[2:3], v[28:29], v[2:3], v[2:3]
	v_min_f32_e32 v30, 0x40e00000, v30
	v_min_f32_e32 v31, 0x40e00000, v31
	v_pk_mul_f32 v[32:33], v[30:31], s[20:21] op_sel_hi:[1,0]
	v_exp_f32_e32 v32, v32
	v_exp_f32_e32 v33, v33
	v_cvt_pk_fp8_f32 v205, v2, v3
	v_pk_fma_f32 v[26:27], v[44:45], v[26:27], v[4:5] op_sel_hi:[1,0,1]
	v_min_f32_e32 v14, 0x40e00000, v14
	v_pk_add_f32 v[2:3], v[32:33], 1.0 op_sel_hi:[1,0]
	v_med3_f32 v26, v26, s37, v176
	v_rcp_f32_e32 v2, v2
	v_rcp_f32_e32 v3, v3
	v_med3_f32 v27, v27, s37, v176
	v_min_f32_e32 v15, 0x40e00000, v15
	v_pk_fma_f32 v[16:17], v[38:39], v[22:23], v[16:17] op_sel_hi:[1,0,1]
	v_pk_mul_f32 v[2:3], v[30:31], v[2:3]
	v_med3_f32 v16, v16, s37, v176
	v_pk_fma_f32 v[2:3], v[26:27], v[2:3], v[2:3]
	v_cvt_pk_fp8_f32 v205, v2, v3 op_sel:[0,0,1]
	v_pk_mul_f32 v[28:29], v[24:25], s[20:21] op_sel_hi:[1,0]
	v_exp_f32_e32 v28, v28
	v_exp_f32_e32 v29, v29
	s_mov_b32 s28, 0x28000
	v_lshl_add_u64 v[26:27], v[188:189], 0, s[28:29]
	global_store_dwordx2 v[26:27], v[204:205], off
	v_pk_add_f32 v[2:3], v[28:29], 1.0 op_sel_hi:[1,0]
	v_med3_f32 v17, v17, s37, v176
	v_rcp_f32_e32 v2, v2
	v_rcp_f32_e32 v3, v3
	v_pk_fma_f32 v[10:11], v[66:67], v[22:23], v[10:11] op_sel_hi:[1,0,1]
	v_pk_fma_f32 v[12:13], v[40:41], v[22:23], v[12:13] op_sel_hi:[1,0,1]
	v_min_f32_e32 v10, 0x40e00000, v10
	v_pk_mul_f32 v[2:3], v[24:25], v[2:3]
	v_pk_mul_f32 v[24:25], v[14:15], s[20:21] op_sel_hi:[1,0]
	v_pk_fma_f32 v[2:3], v[16:17], v[2:3], v[2:3]
	v_exp_f32_e32 v24, v24
	v_exp_f32_e32 v25, v25
	v_cvt_pk_fp8_f32 v206, v2, v3
	v_min_f32_e32 v11, 0x40e00000, v11
	v_pk_add_f32 v[2:3], v[24:25], 1.0 op_sel_hi:[1,0]
	v_med3_f32 v12, v12, s37, v176
	v_rcp_f32_e32 v2, v2
	v_rcp_f32_e32 v3, v3
	v_med3_f32 v13, v13, s37, v176
	v_pk_fma_f32 v[6:7], v[68:69], v[22:23], v[6:7] op_sel_hi:[1,0,1]
	v_pk_fma_f32 v[8:9], v[34:35], v[22:23], v[8:9] op_sel_hi:[1,0,1]
	v_pk_mul_f32 v[2:3], v[14:15], v[2:3]
	v_pk_mul_f32 v[14:15], v[10:11], s[20:21] op_sel_hi:[1,0]
	v_pk_fma_f32 v[2:3], v[12:13], v[2:3], v[2:3]
	v_exp_f32_e32 v14, v14
	v_exp_f32_e32 v15, v15
	v_cvt_pk_fp8_f32 v206, v2, v3 op_sel:[0,0,1]
	v_min_f32_e32 v6, 0x40e00000, v6
	v_pk_add_f32 v[2:3], v[14:15], 1.0 op_sel_hi:[1,0]
	v_min_f32_e32 v7, 0x40e00000, v7
	v_rcp_f32_e32 v2, v2
	v_rcp_f32_e32 v3, v3
	v_med3_f32 v8, v8, s37, v176
	v_med3_f32 v9, v9, s37, v176
	v_pk_fma_f32 v[4:5], v[36:37], v[22:23], v[4:5] op_sel_hi:[1,0,1]
	v_pk_mul_f32 v[2:3], v[10:11], v[2:3]
	v_pk_mul_f32 v[10:11], v[6:7], s[20:21] op_sel_hi:[1,0]
	v_pk_fma_f32 v[2:3], v[8:9], v[2:3], v[2:3]
	v_exp_f32_e32 v10, v10
	v_exp_f32_e32 v11, v11
	v_cvt_pk_fp8_f32 v207, v2, v3
	v_med3_f32 v4, v4, s37, v176
	v_pk_add_f32 v[2:3], v[10:11], 1.0 op_sel_hi:[1,0]
	v_med3_f32 v5, v5, s37, v176
	v_rcp_f32_e32 v2, v2
	v_rcp_f32_e32 v3, v3
	s_nop 0
	v_pk_mul_f32 v[2:3], v[6:7], v[2:3]
	s_nop 0
	v_pk_fma_f32 v[2:3], v[4:5], v[2:3], v[2:3]
	v_cvt_pk_fp8_f32 v207, v2, v3 op_sel:[0,0,1]
	s_mov_b32 s28, 0x2c000
	v_lshl_add_u64 v[4:5], v[188:189], 0, s[28:29]
	global_store_dwordx2 v[4:5], v[206:207], off
	s_cbranch_vccnz .LBB0_1920
	s_andn2_b64 vcc, exec, s[0:1]
	s_cbranch_vccnz .LBB0_1919
	s_barrier
